# baseline (speedup 1.0000x reference)
.LBB5_176:
	s_or_b64 exec, exec, s[2:3]
	v_mov_b32_e32 v2, 0
	s_waitcnt lgkmcnt(0)
	s_barrier
	ds_read_b32 v2, v2
	s_waitcnt lgkmcnt(0)
	v_cmp_eq_u32_e32 vcc, 0, v2
	s_cbranch_vccnz .LBB5_184
	s_movk_i32 s2, 0x80
	v_cmp_gt_u32_e32 vcc, s2, v0
	v_lshl_add_u32 v20, v0, 2, 0
	s_and_saveexec_b64 s[2:3], vcc
	s_cbranch_execz .LBB5_180
	s_and_b32 s4, s34, 0xffffffe
	v_or_b32_e32 v3, s4, v187
	v_lshlrev_b32_e32 v4, 4, v3
	v_lshl_add_u32 v2, v187, 2, 0
	v_ashrrev_i32_e32 v5, 31, v4
	v_add_u32_e32 v2, 0x22200, v2
	v_lshl_add_u64 v[4:5], v[4:5], 2, s[22:23]
	ds_read_b32 v2, v2
	global_load_dword v21, v[4:5], off sc1
	global_load_dword v15, v[4:5], off offset:4 sc1
	global_load_dword v32, v[4:5], off offset:8 sc1
	global_load_dword v17, v[4:5], off offset:12 sc1
	global_load_dword v33, v[4:5], off offset:16 sc1
	global_load_dword v19, v[4:5], off offset:20 sc1
	global_load_dword v34, v[4:5], off offset:24 sc1
	global_load_dword v23, v[4:5], off offset:28 sc1
	global_load_dword v35, v[4:5], off offset:32 sc1
	global_load_dword v25, v[4:5], off offset:36 sc1
	global_load_dword v36, v[4:5], off offset:40 sc1
	global_load_dword v27, v[4:5], off offset:44 sc1
	global_load_dword v37, v[4:5], off offset:48 sc1
	global_load_dword v29, v[4:5], off offset:52 sc1
	global_load_dword v38, v[4:5], off offset:56 sc1
	v_and_or_b32 v6, s34, -2, v187
	v_ashrrev_i32_e32 v7, 31, v6
	v_lshlrev_b64 v[6:7], 11, v[6:7]
	v_mov_b32_e32 v11, 0
	v_lshl_add_u64 v[6:7], s[20:21], 0, v[6:7]
	v_lshl_add_u64 v[6:7], v[6:7], 0, v[10:11]
	global_load_dword v31, v[4:5], off offset:60 sc1
	global_load_dword v14, v[6:7], off sc1
	global_load_dword v16, v[6:7], off offset:256 sc1
	global_load_dword v18, v[6:7], off offset:512 sc1
	global_load_dword v22, v[6:7], off offset:768 sc1
	global_load_dword v24, v[6:7], off offset:1024 sc1
	global_load_dword v26, v[6:7], off offset:1280 sc1
	global_load_dword v28, v[6:7], off offset:1536 sc1
	global_load_dword v30, v[6:7], off offset:1792 sc1
	s_waitcnt lgkmcnt(0)
	v_lshl_or_b32 v4, v2, 6, v189
	v_ashrrev_i32_e32 v5, 31, v4
	v_ashrrev_i32_e32 v3, 31, v2
	v_lshl_add_u64 v[4:5], v[4:5], 2, s[36:37]
	v_lshlrev_b64 v[6:7], 11, v[2:3]
	global_load_dword v3, v[4:5], off
	v_mov_b32_e32 v13, v11
	v_lshl_add_u64 v[6:7], s[38:39], 0, v[6:7]
	v_lshl_add_u64 v[12:13], v[6:7], 0, v[12:13]
	global_load_dwordx4 v[4:7], v[12:13], off
	global_load_dwordx4 v[8:11], v[12:13], off offset:16
	v_lshlrev_b32_e32 v208, 5, v2
	global_load_dwordx4 v[200:203], v208, s[10:11]
	global_load_dwordx4 v[204:207], v208, s[10:11] offset:16
	s_mov_b32 s4, 0xff61b1e6
	s_waitcnt vmcnt(26)
	v_max3_f32 v12, v21, s4, v32
	s_waitcnt vmcnt(22)
	v_max3_f32 v12, v12, v33, v34
	s_waitcnt vmcnt(18)
	v_max3_f32 v12, v12, v35, v36
	s_waitcnt vmcnt(14)
	v_max3_f32 v12, v12, v37, v38
	v_sub_f32_e32 v13, v21, v12
	v_sub_f32_e32 v21, v32, v12
	v_sub_f32_e32 v32, v33, v12
	v_sub_f32_e32 v33, v34, v12
	v_sub_f32_e32 v34, v35, v12
	v_sub_f32_e32 v35, v36, v12
	v_sub_f32_e32 v36, v37, v12
	v_sub_f32_e32 v12, v38, v12
	v_mul_f32_e32 v13, 0x3fb8aa3b, v13
	v_mul_f32_e32 v21, 0x3fb8aa3b, v21
	v_mul_f32_e32 v41, 0x3fb8aa3b, v12
	v_exp_f32_e32 v12, v13
	v_mul_f32_e32 v37, 0x3fb8aa3b, v32
	v_exp_f32_e32 v32, v21
	v_mul_f32_e32 v33, 0x3fb8aa3b, v33
	v_mul_f32_e32 v38, 0x3fb8aa3b, v34
	v_exp_f32_e32 v34, v37
	v_mul_f32_e32 v39, 0x3fb8aa3b, v36
	v_exp_f32_e32 v36, v33
	v_mul_f32_e32 v35, 0x3fb8aa3b, v35
	v_exp_f32_e32 v38, v38
	s_waitcnt vmcnt(12)
	v_pk_fma_f32 v[12:13], v[12:13], v[14:15], 0 op_sel_hi:[0,1,0]
	v_exp_f32_e32 v40, v35
	s_waitcnt vmcnt(11)
	v_pk_fma_f32 v[12:13], v[32:33], v[16:17], v[12:13] op_sel_hi:[0,1,1]
	v_exp_f32_e32 v42, v39
	s_waitcnt vmcnt(10)
	v_pk_fma_f32 v[12:13], v[34:35], v[18:19], v[12:13] op_sel_hi:[0,1,1]
	v_exp_f32_e32 v44, v41
	s_waitcnt vmcnt(9)
	v_pk_fma_f32 v[12:13], v[36:37], v[22:23], v[12:13] op_sel_hi:[0,1,1]
	s_waitcnt vmcnt(8)
	v_pk_fma_f32 v[12:13], v[38:39], v[24:25], v[12:13] op_sel_hi:[0,1,1]
	s_waitcnt vmcnt(7)
	v_pk_fma_f32 v[12:13], v[40:41], v[26:27], v[12:13] op_sel_hi:[0,1,1]
	s_waitcnt vmcnt(6)
	v_pk_fma_f32 v[12:13], v[42:43], v[28:29], v[12:13] op_sel_hi:[0,1,1]
	s_waitcnt vmcnt(5)
	v_pk_fma_f32 v[12:13], v[44:45], v[30:31], v[12:13] op_sel_hi:[0,1,1]
	v_div_scale_f32 v14, s[4:5], v13, v13, v12
	v_rcp_f32_e32 v15, v14
	v_div_scale_f32 v16, vcc, v12, v13, v12
	v_fma_f32 v17, -v14, v15, 1.0
	v_fmac_f32_e32 v15, v17, v15
	v_mul_f32_e32 v17, v16, v15
	v_fma_f32 v18, -v14, v17, v16
	v_fmac_f32_e32 v17, v18, v15
	v_fma_f32 v14, -v14, v17, v16
	v_div_fmas_f32 v14, v14, v15, v17
	v_div_fixup_f32 v12, v14, v13, v12
	s_waitcnt vmcnt(4)
	v_add_f32_e32 v3, v12, v3
	v_max_f32_e32 v22, 0, v3
	ds_write_b32 v20, v22 offset:1024
	v_mov_b32_e32 v23, v22
	s_waitcnt vmcnt(2)
	v_pk_mul_f32 v[12:13], v[22:23], v[4:5]
	v_pk_mul_f32 v[14:15], v[22:23], v[6:7]
	v_pk_mul_f32 v[16:17], v[22:23], v[8:9]
	v_pk_mul_f32 v[18:19], v[22:23], v[10:11]
	v_add_f32_dpp v12, v12, v12 quad_perm:[1,0,3,2] row_mask:0xf bank_mask:0xf
	v_add_f32_dpp v13, v13, v13 quad_perm:[1,0,3,2] row_mask:0xf bank_mask:0xf
	v_add_f32_dpp v14, v14, v14 quad_perm:[1,0,3,2] row_mask:0xf bank_mask:0xf
	v_add_f32_dpp v15, v15, v15 quad_perm:[1,0,3,2] row_mask:0xf bank_mask:0xf
	v_add_f32_dpp v16, v16, v16 quad_perm:[1,0,3,2] row_mask:0xf bank_mask:0xf
	v_add_f32_dpp v17, v17, v17 quad_perm:[1,0,3,2] row_mask:0xf bank_mask:0xf
	v_add_f32_dpp v18, v18, v18 quad_perm:[1,0,3,2] row_mask:0xf bank_mask:0xf
	v_add_f32_dpp v19, v19, v19 quad_perm:[1,0,3,2] row_mask:0xf bank_mask:0xf
	v_add_f32_dpp v12, v12, v12 quad_perm:[2,3,0,1] row_mask:0xf bank_mask:0xf
	v_add_f32_dpp v13, v13, v13 quad_perm:[2,3,0,1] row_mask:0xf bank_mask:0xf
	v_add_f32_dpp v14, v14, v14 quad_perm:[2,3,0,1] row_mask:0xf bank_mask:0xf
	v_add_f32_dpp v15, v15, v15 quad_perm:[2,3,0,1] row_mask:0xf bank_mask:0xf
	v_add_f32_dpp v16, v16, v16 quad_perm:[2,3,0,1] row_mask:0xf bank_mask:0xf
	v_add_f32_dpp v17, v17, v17 quad_perm:[2,3,0,1] row_mask:0xf bank_mask:0xf
	v_add_f32_dpp v18, v18, v18 quad_perm:[2,3,0,1] row_mask:0xf bank_mask:0xf
	v_add_f32_dpp v19, v19, v19 quad_perm:[2,3,0,1] row_mask:0xf bank_mask:0xf
	v_add_f32_dpp v12, v12, v12 row_half_mirror row_mask:0xf bank_mask:0xf
	v_add_f32_dpp v13, v13, v13 row_half_mirror row_mask:0xf bank_mask:0xf
	v_add_f32_dpp v14, v14, v14 row_half_mirror row_mask:0xf bank_mask:0xf
	v_add_f32_dpp v15, v15, v15 row_half_mirror row_mask:0xf bank_mask:0xf
	v_add_f32_dpp v16, v16, v16 row_half_mirror row_mask:0xf bank_mask:0xf
	v_add_f32_dpp v17, v17, v17 row_half_mirror row_mask:0xf bank_mask:0xf
	v_add_f32_dpp v18, v18, v18 row_half_mirror row_mask:0xf bank_mask:0xf
	v_add_f32_dpp v19, v19, v19 row_half_mirror row_mask:0xf bank_mask:0xf
	v_add_f32_dpp v12, v12, v12 row_mirror row_mask:0xf bank_mask:0xf
	v_add_f32_dpp v13, v13, v13 row_mirror row_mask:0xf bank_mask:0xf
	v_add_f32_dpp v14, v14, v14 row_mirror row_mask:0xf bank_mask:0xf
	v_add_f32_dpp v15, v15, v15 row_mirror row_mask:0xf bank_mask:0xf
	v_add_f32_dpp v16, v16, v16 row_mirror row_mask:0xf bank_mask:0xf
	v_add_f32_dpp v17, v17, v17 row_mirror row_mask:0xf bank_mask:0xf
	v_add_f32_dpp v18, v18, v18 row_mirror row_mask:0xf bank_mask:0xf
	v_add_f32_dpp v19, v19, v19 row_mirror row_mask:0xf bank_mask:0xf
	ds_bpermute_b32 v24, v181, v12
	ds_bpermute_b32 v25, v181, v13
	ds_bpermute_b32 v26, v181, v14
	ds_bpermute_b32 v27, v181, v15
	ds_bpermute_b32 v28, v181, v16
	ds_bpermute_b32 v29, v181, v17
	ds_bpermute_b32 v30, v181, v18
	ds_bpermute_b32 v31, v181, v19
	s_waitcnt lgkmcnt(0)
	v_pk_add_f32 v[12:13], v[12:13], v[24:25]
	v_pk_add_f32 v[14:15], v[14:15], v[26:27]
	v_pk_add_f32 v[16:17], v[16:17], v[28:29]
	v_pk_add_f32 v[18:19], v[18:19], v[30:31]
	ds_bpermute_b32 v24, v183, v12
	ds_bpermute_b32 v25, v183, v13
	ds_bpermute_b32 v26, v183, v14
	ds_bpermute_b32 v27, v183, v15
	ds_bpermute_b32 v28, v183, v16
	ds_bpermute_b32 v29, v183, v17
	ds_bpermute_b32 v30, v183, v18
	ds_bpermute_b32 v31, v183, v19
	s_waitcnt lgkmcnt(0)
	v_pk_add_f32 v[12:13], v[12:13], v[24:25]
	v_pk_add_f32 v[14:15], v[14:15], v[26:27]
	v_pk_add_f32 v[16:17], v[16:17], v[28:29]
	v_pk_add_f32 v[18:19], v[18:19], v[30:31]
	v_cmp_eq_u32_e32 vcc, 0, v189
	s_and_b64 exec, exec, vcc
	s_cbranch_execz .LBB5_180
	s_waitcnt vmcnt(0)
	v_pk_add_f32 v[12:13], v[12:13], v[200:201]
	v_pk_add_f32 v[14:15], v[14:15], v[202:203]
	v_pk_add_f32 v[16:17], v[16:17], v[204:205]
	v_pk_add_f32 v[18:19], v[18:19], v[206:207]
	v_add_u32_e32 v1, 0, v146
	ds_write_b128 v1, v[12:15] offset:1536
	ds_write_b128 v1, v[16:19] offset:1552
